# plus: out-proj epilogue bf16 path without the per-row-group gate drain; attention waves 4-7 at priority 1
# speedup vs baseline: 1.0460x; 1.0101x over previous
.LBB0_487:
	s_ashr_i32 s0, s2, 31
	s_lshr_b32 s0, s0, 28
	s_add_i32 s0, s2, s0
	s_ashr_i32 s18, s0, 4
	s_and_b32 s0, s0, -16
	s_sub_i32 s3, s2, s0
	s_sub_i32 s22, 31, s3
	s_mul_i32 s1, s18, 0x180000
	v_readlane_b32 s12, v253, 19
	s_mul_hi_i32 s0, s18, 0x180000
	v_readlane_b32 s13, v253, 20
	s_add_u32 s14, s12, s1
	s_addc_u32 s15, s13, s0
	v_readlane_b32 s12, v253, 15
	v_mov_b32_e32 v22, v0
	v_mov_b32_e32 v18, v224
	v_readlane_b32 s25, v251, 36
	s_cmp_lt_u32 s25, 4
	s_cbranch_scc1 .Lprio_skip_a
	s_setprio 1
.Lprio_skip_a:
	v_readlane_b32 s13, v253, 16
	s_add_u32 s12, s12, s1
	s_addc_u32 s13, s13, s0
	s_lshl_b32 s0, s22, 8
	s_lshl_b32 s1, s25, 5
	v_and_b32_e32 v193, 31, v18
	v_ashrrev_i32_e32 v36, 5, v18
	s_add_i32 s1, s1, s0
	v_or_b32_e32 v151, s1, v193
	v_mov_b64_e32 v[18:19], s[14:15]
	v_lshlrev_b32_e32 v160, 3, v36
	v_mad_i64_i32 v[18:19], s[0:1], v151, s8, v[18:19]
	v_ashrrev_i32_e32 v161, 31, v160
	v_lshl_add_u64 v[18:19], v[160:161], 1, v[18:19]
	s_mov_b32 s16, 0x2aaaaaab
	global_load_dwordx4 v[144:147], v[18:19], off
	global_load_dwordx4 v[140:143], v[18:19], off offset:32
	global_load_dwordx4 v[136:139], v[18:19], off offset:64
	global_load_dwordx4 v[132:135], v[18:19], off offset:96
	global_load_dwordx4 v[128:131], v[18:19], off offset:128
	global_load_dwordx4 v[124:127], v[18:19], off offset:160
	v_mul_hi_i32 v18, v22, s16
	v_lshrrev_b32_e32 v19, 31, v18
	v_ashrrev_i32_e32 v18, 1, v18
	v_add_u32_e32 v161, v18, v19
	v_mul_lo_u32 v18, v161, 12
	v_sub_u32_e32 v37, v22, v18
	v_mov_b64_e32 v[18:19], s[12:13]
	v_lshlrev_b32_e32 v156, 3, v37
	v_mad_i64_i32 v[18:19], s[0:1], v161, s8, v[18:19]
	v_ashrrev_i32_e32 v157, 31, v156
	v_lshl_add_u64 v[18:19], v[156:157], 1, v[18:19]
	global_load_dwordx4 v[18:21], v[18:19], off
	v_add_u32_e32 v23, 0x200, v22
	v_mul_hi_i32 v24, v23, s16
	v_lshrrev_b32_e32 v25, 31, v24
	v_ashrrev_i32_e32 v24, 1, v24
	v_add_u32_e32 v187, v24, v25
	v_mul_lo_u32 v24, v187, 12
	v_sub_u32_e32 v191, v23, v24
	s_movk_i32 s0, 0xff
	s_movk_i32 s16, 0x100
	v_lshlrev_b32_e32 v154, 3, v191
	v_cmp_lt_i32_e64 s[0:1], s0, v22
	v_cmp_gt_i32_e64 s[38:39], s16, v22
	v_ashrrev_i32_e32 v155, 31, v154
	s_and_saveexec_b64 s[16:17], s[38:39]
	s_cbranch_execz .LBB0_489
	v_mov_b64_e32 v[24:25], s[12:13]
	v_mad_i64_i32 v[24:25], s[20:21], v187, s8, v[24:25]
	v_lshl_add_u64 v[24:25], v[154:155], 1, v[24:25]
	global_load_dwordx4 v[116:119], v[24:25], off

.LBB0_911:
	s_or_b64 exec, exec, s[0:1]
	s_setprio 0
	v_readlane_b32 s0, v253, 21
	v_readlane_b32 s1, v253, 22
	s_andn2_b64 vcc, exec, s[0:1]
	s_barrier
	s_cbranch_vccnz .LBB0_1005
	v_readlane_b32 s12, v254, 51
	s_add_i32 s80, s12, 1
	s_cmp_lg_u32 s12, 3
	s_cselect_b64 s[56:57], -1, 0
	s_lshl_b64 s[0:1], s[80:81], 14
	s_lshl_b64 s[2:3], s[80:81], 17
	s_bitcmp1_b32 s80, 0
	s_mov_b64 s[30:31], s[76:77]
	v_readlane_b32 s36, v251, 20
	s_cselect_b32 s29, s85, 0x713d000
	s_cselect_b32 s27, 0x66f0000, 0
	s_lshl_b64 s[34:35], s[80:81], 16
	s_lshl_b64 s[52:53], s[80:81], 18
	s_lshl_b64 s[54:55], s[80:81], 22
	s_lshl_b64 s[90:91], s[80:81], 26
	s_lshl_b32 s85, s12, 8
	s_lshl_b32 s31, s12, 6
	v_readlane_b32 s50, v251, 34
	v_readlane_b32 s37, v251, 21
	v_readlane_b32 s51, v251, 35
	s_add_u32 s36, s50, s0
	s_addc_u32 s37, s51, s1
	s_add_u32 s76, s62, s2
	s_addc_u32 s77, s63, s3
	s_add_u32 s0, s74, s27
	v_readlane_b32 s12, v251, 39
	s_addc_u32 s1, s75, 0
	v_readlane_b32 s24, v251, 51
	v_readlane_b32 s25, v251, 52
	s_add_u32 s2, s24, s34
	s_addc_u32 s3, s25, s35
	v_readlane_b32 s18, v251, 45
	v_writelane_b32 v255, s3, 0
	s_add_u32 s3, s0, 0x1135000
	v_writelane_b32 v255, s3, 1
	s_addc_u32 s3, s1, 0
	v_readlane_b32 s19, v251, 46
	v_writelane_b32 v255, s3, 2
	s_add_u32 s3, s18, s52
	v_writelane_b32 v255, s3, 3
	s_addc_u32 s3, s19, s53
	v_writelane_b32 v255, s3, 4
	s_mov_b32 s19, s2
	s_add_u32 s2, s0, 0x1115000
	s_mul_i32 s28, s80, 0x48000
	v_readlane_b32 s14, v251, 41
	v_writelane_b32 v255, s2, 5
	s_addc_u32 s2, s1, 0
	v_writelane_b32 v255, s2, 6
	s_add_u32 s2, s14, s28
	v_readlane_b32 s15, v251, 42
	v_writelane_b32 v255, s2, 7
	s_mul_hi_u32 s2, s80, 0x48000
	s_addc_u32 s2, s15, s2
	v_writelane_b32 v255, s2, 8
	s_add_u32 s2, s0, 0x10f1000
	v_readlane_b32 s48, v251, 32
	v_writelane_b32 v255, s2, 9
	s_addc_u32 s2, s1, 0
	v_readlane_b32 s49, v251, 33
	v_writelane_b32 v255, s2, 10
	s_add_u32 s2, s48, s54
	v_readlane_b32 s40, v251, 24
	v_readlane_b32 s41, v251, 25
	v_readlane_b32 s42, v251, 26
	v_readlane_b32 s43, v251, 27
	v_readlane_b32 s44, v251, 28
	v_readlane_b32 s45, v251, 29
	v_readlane_b32 s46, v251, 30
	v_readlane_b32 s47, v251, 31
	v_writelane_b32 v255, s2, 11
	s_addc_u32 s2, s49, s55
	v_writelane_b32 v255, s2, 12
	s_add_u32 s3, s0, 0xef1000
	v_readlane_b32 s40, v251, 4
	s_mul_i32 s2, s80, 0x860000
	v_writelane_b32 v255, s3, 13
	s_addc_u32 s3, s1, 0
	v_readlane_b32 s54, v251, 18
	v_writelane_b32 v255, s3, 14
	s_add_u32 s2, s54, s2
	v_readlane_b32 s55, v251, 19
	v_writelane_b32 v255, s2, 15
	s_mul_hi_u32 s2, s80, 0x860000
	s_addc_u32 s2, s55, s2
	v_writelane_b32 v255, s2, 16
	s_add_u32 s2, s0, 0xa71000
	v_readlane_b32 s20, v251, 47
	v_writelane_b32 v255, s2, 17
	s_addc_u32 s2, s1, 0
	v_readlane_b32 s21, v251, 48
	s_add_u32 s20, s70, s90
	s_addc_u32 s21, s71, s91
	v_readlane_b32 s13, v251, 40
	s_add_u32 s12, s0, 0x513d000
	s_addc_u32 s13, s1, 0
	s_add_u32 s82, s0, 0x113d000
	s_addc_u32 s88, s1, 0
	s_add_u32 s0, s74, s29
	v_writelane_b32 v255, s2, 18
	s_addc_u32 s1, s75, 0
	v_readlane_b32 s16, v251, 43
	v_readlane_b32 s17, v251, 44
	v_writelane_b32 v255, s0, 19
	s_mov_b64 s[16:17], s[56:57]
	s_mov_b32 s18, s31
	v_writelane_b32 v255, s1, 20
	v_readlane_b32 s89, v254, 19
	s_mov_b32 s2, s30
	v_readlane_b32 s38, v251, 22
	v_readlane_b32 s39, v251, 23
	v_readlane_b32 s22, v251, 49
	v_readlane_b32 s23, v251, 50
	v_readlane_b32 s26, v251, 53
	v_readlane_b32 s27, v251, 54
	v_readlane_b32 s41, v251, 5
	v_readlane_b32 s42, v251, 6
	v_readlane_b32 s43, v251, 7
	v_readlane_b32 s44, v251, 8
	v_readlane_b32 s45, v251, 9
	v_readlane_b32 s46, v251, 10
	v_readlane_b32 s47, v251, 11
	v_readlane_b32 s48, v251, 12
	v_readlane_b32 s49, v251, 13
	v_readlane_b32 s50, v251, 14
	v_readlane_b32 s51, v251, 15
	v_readlane_b32 s52, v251, 16
	v_readlane_b32 s53, v251, 17
	s_branch .LBB0_914

.LBB0_1077:
	v_readlane_b32 s76, v254, 60
	s_andn2_b64 vcc, exec, s[30:31]
	v_readlane_b32 s77, v254, 61
	s_cbranch_vccnz .LBB0_1079
	v_lshlrev_b64 v[140:141], 1, v[168:169]
	v_lshl_add_u64 v[142:143], s[92:93], 0, v[140:141]
	v_lshl_add_u64 v[140:141], s[4:5], 0, v[140:141]
	global_load_dwordx4 v[142:145], v[142:143], off
	s_nop 0
	global_load_dwordx4 v[174:177], v[140:141], off
	s_waitcnt vmcnt(1)
	v_lshlrev_b32_e32 v140, 16, v142
	v_and_b32_e32 v141, 0xffff0000, v142
	v_lshlrev_b32_e32 v142, 16, v143
	v_and_b32_e32 v143, 0xffff0000, v143
	s_waitcnt vmcnt(0)
	v_lshlrev_b32_e32 v146, 16, v174
	v_and_b32_e32 v147, 0xffff0000, v174
	v_lshlrev_b32_e32 v174, 16, v175
	v_and_b32_e32 v175, 0xffff0000, v175
	v_pk_add_f32 v[142:143], v[142:143], v[174:175]
	v_pk_add_f32 v[140:141], v[140:141], v[146:147]
	v_lshlrev_b32_e32 v174, 16, v144
	v_and_b32_e32 v175, 0xffff0000, v144
	v_lshlrev_b32_e32 v144, 16, v145
	v_and_b32_e32 v145, 0xffff0000, v145
	v_lshlrev_b32_e32 v178, 16, v176
	v_and_b32_e32 v179, 0xffff0000, v176
	v_lshlrev_b32_e32 v146, 16, v177
	v_and_b32_e32 v147, 0xffff0000, v177
	v_pk_add_f32 v[146:147], v[144:145], v[146:147]
	v_pk_add_f32 v[144:145], v[174:175], v[178:179]

.LBB0_1082:
	v_or_b32_e32 v140, 0x80, v158
	v_ashrrev_i32_e32 v141, 31, v140
	s_andn2_b64 vcc, exec, s[30:31]
	v_lshl_add_u64 v[142:143], v[162:163], 0, v[140:141]
	s_cbranch_vccnz .LBB0_1084
	v_lshlrev_b64 v[132:133], 1, v[142:143]
	v_lshl_add_u64 v[134:135], s[92:93], 0, v[132:133]
	v_lshl_add_u64 v[132:133], s[4:5], 0, v[132:133]
	global_load_dwordx4 v[134:137], v[134:135], off
	s_nop 0
	global_load_dwordx4 v[144:147], v[132:133], off
	s_waitcnt vmcnt(1)
	v_lshlrev_b32_e32 v132, 16, v134
	v_and_b32_e32 v133, 0xffff0000, v134
	v_lshlrev_b32_e32 v134, 16, v135
	v_and_b32_e32 v135, 0xffff0000, v135
	s_waitcnt vmcnt(0)
	v_lshlrev_b32_e32 v138, 16, v144
	v_and_b32_e32 v139, 0xffff0000, v144
	v_lshlrev_b32_e32 v144, 16, v145
	v_and_b32_e32 v145, 0xffff0000, v145
	v_pk_add_f32 v[134:135], v[134:135], v[144:145]
	v_pk_add_f32 v[132:133], v[132:133], v[138:139]
	v_lshlrev_b32_e32 v144, 16, v136
	v_and_b32_e32 v145, 0xffff0000, v136
	v_lshlrev_b32_e32 v136, 16, v137
	v_and_b32_e32 v137, 0xffff0000, v137
	v_lshlrev_b32_e32 v162, 16, v146
	v_and_b32_e32 v163, 0xffff0000, v146
	v_lshlrev_b32_e32 v138, 16, v147
	v_and_b32_e32 v139, 0xffff0000, v147
	v_pk_add_f32 v[138:139], v[136:137], v[138:139]
	v_pk_add_f32 v[136:137], v[144:145], v[162:163]

.LBB0_1086:
	v_lshlrev_b64 v[124:125], 1, v[138:139]
	v_lshl_add_u64 v[126:127], s[92:93], 0, v[124:125]
	v_lshl_add_u64 v[124:125], s[4:5], 0, v[124:125]
	global_load_dwordx4 v[126:129], v[126:127], off
	s_nop 0
	global_load_dwordx4 v[142:145], v[124:125], off
	s_waitcnt vmcnt(1)
	v_lshlrev_b32_e32 v124, 16, v126
	v_and_b32_e32 v125, 0xffff0000, v126
	v_lshlrev_b32_e32 v126, 16, v127
	v_and_b32_e32 v127, 0xffff0000, v127
	s_waitcnt vmcnt(0)
	v_lshlrev_b32_e32 v130, 16, v142
	v_and_b32_e32 v131, 0xffff0000, v142
	v_lshlrev_b32_e32 v142, 16, v143
	v_and_b32_e32 v143, 0xffff0000, v143
	v_pk_add_f32 v[126:127], v[126:127], v[142:143]
	v_pk_add_f32 v[124:125], v[124:125], v[130:131]
	v_lshlrev_b32_e32 v142, 16, v128
	v_and_b32_e32 v143, 0xffff0000, v128
	v_lshlrev_b32_e32 v128, 16, v129
	v_and_b32_e32 v129, 0xffff0000, v129
	v_lshlrev_b32_e32 v146, 16, v144
	v_and_b32_e32 v147, 0xffff0000, v144
	v_lshlrev_b32_e32 v130, 16, v145
	v_and_b32_e32 v131, 0xffff0000, v145
	v_pk_add_f32 v[130:131], v[128:129], v[130:131]
	v_pk_add_f32 v[128:129], v[142:143], v[146:147]

.LBB0_1089:
	v_lshlrev_b64 v[116:117], 1, v[124:125]
	v_lshl_add_u64 v[118:119], s[92:93], 0, v[116:117]
	v_lshl_add_u64 v[116:117], s[4:5], 0, v[116:117]
	global_load_dwordx4 v[118:121], v[118:119], off
	s_nop 0
	global_load_dwordx4 v[126:129], v[116:117], off
	s_waitcnt vmcnt(1)
	v_lshlrev_b32_e32 v116, 16, v118
	v_and_b32_e32 v117, 0xffff0000, v118
	v_lshlrev_b32_e32 v118, 16, v119
	v_and_b32_e32 v119, 0xffff0000, v119
	s_waitcnt vmcnt(0)
	v_lshlrev_b32_e32 v122, 16, v126
	v_and_b32_e32 v123, 0xffff0000, v126
	v_lshlrev_b32_e32 v126, 16, v127
	v_and_b32_e32 v127, 0xffff0000, v127
	v_pk_add_f32 v[118:119], v[118:119], v[126:127]
	v_pk_add_f32 v[116:117], v[116:117], v[122:123]
	v_lshlrev_b32_e32 v126, 16, v120
	v_and_b32_e32 v127, 0xffff0000, v120
	v_lshlrev_b32_e32 v120, 16, v121
	v_and_b32_e32 v121, 0xffff0000, v121
	v_lshlrev_b32_e32 v130, 16, v128
	v_and_b32_e32 v131, 0xffff0000, v128
	v_lshlrev_b32_e32 v122, 16, v129
	v_and_b32_e32 v123, 0xffff0000, v129
	v_pk_add_f32 v[122:123], v[120:121], v[122:123]
	v_pk_add_f32 v[120:121], v[126:127], v[130:131]

.LBB0_1092:
	v_lshlrev_b64 v[106:107], 1, v[122:123]
	v_lshl_add_u64 v[108:109], s[92:93], 0, v[106:107]
	v_lshl_add_u64 v[106:107], s[4:5], 0, v[106:107]
	global_load_dwordx4 v[108:111], v[108:109], off
	s_nop 0
	global_load_dwordx4 v[124:127], v[106:107], off
	s_waitcnt vmcnt(1)
	v_lshlrev_b32_e32 v106, 16, v108
	v_and_b32_e32 v107, 0xffff0000, v108
	v_lshlrev_b32_e32 v108, 16, v109
	v_and_b32_e32 v109, 0xffff0000, v109
	s_waitcnt vmcnt(0)
	v_lshlrev_b32_e32 v112, 16, v124
	v_and_b32_e32 v113, 0xffff0000, v124
	v_lshlrev_b32_e32 v124, 16, v125
	v_and_b32_e32 v125, 0xffff0000, v125
	v_pk_add_f32 v[108:109], v[108:109], v[124:125]
	v_pk_add_f32 v[106:107], v[106:107], v[112:113]
	v_lshlrev_b32_e32 v124, 16, v110
	v_and_b32_e32 v125, 0xffff0000, v110
	v_lshlrev_b32_e32 v110, 16, v111
	v_and_b32_e32 v111, 0xffff0000, v111
	v_lshlrev_b32_e32 v128, 16, v126
	v_and_b32_e32 v129, 0xffff0000, v126
	v_lshlrev_b32_e32 v112, 16, v127
	v_and_b32_e32 v113, 0xffff0000, v127
	v_pk_add_f32 v[112:113], v[110:111], v[112:113]
	v_pk_add_f32 v[110:111], v[124:125], v[128:129]

.LBB0_1095:
	v_lshlrev_b64 v[98:99], 1, v[106:107]
	v_lshl_add_u64 v[100:101], s[92:93], 0, v[98:99]
	v_lshl_add_u64 v[98:99], s[4:5], 0, v[98:99]
	global_load_dwordx4 v[100:103], v[100:101], off
	s_nop 0
	global_load_dwordx4 v[108:111], v[98:99], off
	s_waitcnt vmcnt(1)
	v_lshlrev_b32_e32 v98, 16, v100
	v_and_b32_e32 v99, 0xffff0000, v100
	v_lshlrev_b32_e32 v100, 16, v101
	v_and_b32_e32 v101, 0xffff0000, v101
	s_waitcnt vmcnt(0)
	v_lshlrev_b32_e32 v104, 16, v108
	v_and_b32_e32 v105, 0xffff0000, v108
	v_lshlrev_b32_e32 v108, 16, v109
	v_and_b32_e32 v109, 0xffff0000, v109
	v_pk_add_f32 v[100:101], v[100:101], v[108:109]
	v_pk_add_f32 v[98:99], v[98:99], v[104:105]
	v_lshlrev_b32_e32 v108, 16, v102
	v_and_b32_e32 v109, 0xffff0000, v102
	v_lshlrev_b32_e32 v102, 16, v103
	v_and_b32_e32 v103, 0xffff0000, v103
	v_lshlrev_b32_e32 v112, 16, v110
	v_and_b32_e32 v113, 0xffff0000, v110
	v_lshlrev_b32_e32 v104, 16, v111
	v_and_b32_e32 v105, 0xffff0000, v111
	v_pk_add_f32 v[104:105], v[102:103], v[104:105]
	v_pk_add_f32 v[102:103], v[108:109], v[112:113]

.LBB0_1098:
	v_lshlrev_b64 v[90:91], 1, v[104:105]
	v_lshl_add_u64 v[92:93], s[92:93], 0, v[90:91]
	v_lshl_add_u64 v[90:91], s[4:5], 0, v[90:91]
	global_load_dwordx4 v[92:95], v[92:93], off
	s_nop 0
	global_load_dwordx4 v[106:109], v[90:91], off
	s_waitcnt vmcnt(1)
	v_lshlrev_b32_e32 v90, 16, v92
	v_and_b32_e32 v91, 0xffff0000, v92
	v_lshlrev_b32_e32 v92, 16, v93
	v_and_b32_e32 v93, 0xffff0000, v93
	s_waitcnt vmcnt(0)
	v_lshlrev_b32_e32 v96, 16, v106
	v_and_b32_e32 v97, 0xffff0000, v106
	v_lshlrev_b32_e32 v106, 16, v107
	v_and_b32_e32 v107, 0xffff0000, v107
	v_pk_add_f32 v[92:93], v[92:93], v[106:107]
	v_pk_add_f32 v[90:91], v[90:91], v[96:97]
	v_lshlrev_b32_e32 v106, 16, v94
	v_and_b32_e32 v107, 0xffff0000, v94
	v_lshlrev_b32_e32 v94, 16, v95
	v_and_b32_e32 v95, 0xffff0000, v95
	v_lshlrev_b32_e32 v110, 16, v108
	v_and_b32_e32 v111, 0xffff0000, v108
	v_lshlrev_b32_e32 v96, 16, v109
	v_and_b32_e32 v97, 0xffff0000, v109
	v_pk_add_f32 v[96:97], v[94:95], v[96:97]
	v_pk_add_f32 v[94:95], v[106:107], v[110:111]

.LBB0_1101:
	v_lshlrev_b64 v[82:83], 1, v[90:91]
	v_lshl_add_u64 v[84:85], s[92:93], 0, v[82:83]
	v_lshl_add_u64 v[82:83], s[4:5], 0, v[82:83]
	global_load_dwordx4 v[84:87], v[84:85], off
	s_nop 0
	global_load_dwordx4 v[92:95], v[82:83], off
	s_waitcnt vmcnt(1)
	v_lshlrev_b32_e32 v82, 16, v84
	v_and_b32_e32 v83, 0xffff0000, v84
	v_lshlrev_b32_e32 v84, 16, v85
	v_and_b32_e32 v85, 0xffff0000, v85
	s_waitcnt vmcnt(0)
	v_lshlrev_b32_e32 v88, 16, v92
	v_and_b32_e32 v89, 0xffff0000, v92
	v_lshlrev_b32_e32 v92, 16, v93
	v_and_b32_e32 v93, 0xffff0000, v93
	v_pk_add_f32 v[84:85], v[84:85], v[92:93]
	v_pk_add_f32 v[82:83], v[82:83], v[88:89]
	v_lshlrev_b32_e32 v92, 16, v86
	v_and_b32_e32 v93, 0xffff0000, v86
	v_lshlrev_b32_e32 v86, 16, v87
	v_and_b32_e32 v87, 0xffff0000, v87
	v_lshlrev_b32_e32 v96, 16, v94
	v_and_b32_e32 v97, 0xffff0000, v94
	v_lshlrev_b32_e32 v88, 16, v95
	v_and_b32_e32 v89, 0xffff0000, v95
	v_pk_add_f32 v[88:89], v[86:87], v[88:89]
	v_pk_add_f32 v[86:87], v[92:93], v[96:97]

.LBB0_1104:
	v_lshlrev_b64 v[74:75], 1, v[88:89]
	v_lshl_add_u64 v[76:77], s[92:93], 0, v[74:75]
	v_lshl_add_u64 v[74:75], s[4:5], 0, v[74:75]
	global_load_dwordx4 v[76:79], v[76:77], off
	s_nop 0
	global_load_dwordx4 v[90:93], v[74:75], off
	s_waitcnt vmcnt(1)
	v_lshlrev_b32_e32 v74, 16, v76
	v_and_b32_e32 v75, 0xffff0000, v76
	v_lshlrev_b32_e32 v76, 16, v77
	v_and_b32_e32 v77, 0xffff0000, v77
	s_waitcnt vmcnt(0)
	v_lshlrev_b32_e32 v80, 16, v90
	v_and_b32_e32 v81, 0xffff0000, v90
	v_lshlrev_b32_e32 v90, 16, v91
	v_and_b32_e32 v91, 0xffff0000, v91
	v_pk_add_f32 v[76:77], v[76:77], v[90:91]
	v_pk_add_f32 v[74:75], v[74:75], v[80:81]
	v_lshlrev_b32_e32 v90, 16, v78
	v_and_b32_e32 v91, 0xffff0000, v78
	v_lshlrev_b32_e32 v78, 16, v79
	v_and_b32_e32 v79, 0xffff0000, v79
	v_lshlrev_b32_e32 v94, 16, v92
	v_and_b32_e32 v95, 0xffff0000, v92
	v_lshlrev_b32_e32 v80, 16, v93
	v_and_b32_e32 v81, 0xffff0000, v93
	v_pk_add_f32 v[80:81], v[78:79], v[80:81]
	v_pk_add_f32 v[78:79], v[90:91], v[94:95]

.LBB0_1107:
	v_lshlrev_b64 v[66:67], 1, v[74:75]
	v_lshl_add_u64 v[68:69], s[92:93], 0, v[66:67]
	v_lshl_add_u64 v[66:67], s[4:5], 0, v[66:67]
	global_load_dwordx4 v[68:71], v[68:69], off
	s_nop 0
	global_load_dwordx4 v[76:79], v[66:67], off
	s_waitcnt vmcnt(1)
	v_lshlrev_b32_e32 v66, 16, v68
	v_and_b32_e32 v67, 0xffff0000, v68
	v_lshlrev_b32_e32 v68, 16, v69
	v_and_b32_e32 v69, 0xffff0000, v69
	s_waitcnt vmcnt(0)
	v_lshlrev_b32_e32 v72, 16, v76
	v_and_b32_e32 v73, 0xffff0000, v76
	v_lshlrev_b32_e32 v76, 16, v77
	v_and_b32_e32 v77, 0xffff0000, v77
	v_pk_add_f32 v[68:69], v[68:69], v[76:77]
	v_pk_add_f32 v[66:67], v[66:67], v[72:73]
	v_lshlrev_b32_e32 v76, 16, v70
	v_and_b32_e32 v77, 0xffff0000, v70
	v_lshlrev_b32_e32 v70, 16, v71
	v_and_b32_e32 v71, 0xffff0000, v71
	v_lshlrev_b32_e32 v80, 16, v78
	v_and_b32_e32 v81, 0xffff0000, v78
	v_lshlrev_b32_e32 v72, 16, v79
	v_and_b32_e32 v73, 0xffff0000, v79
	v_pk_add_f32 v[72:73], v[70:71], v[72:73]
	v_pk_add_f32 v[70:71], v[76:77], v[80:81]

.LBB0_1110:
	v_lshlrev_b64 v[58:59], 1, v[72:73]
	v_lshl_add_u64 v[60:61], s[92:93], 0, v[58:59]
	v_lshl_add_u64 v[58:59], s[4:5], 0, v[58:59]
	global_load_dwordx4 v[60:63], v[60:61], off
	s_nop 0
	global_load_dwordx4 v[74:77], v[58:59], off
	s_waitcnt vmcnt(1)
	v_lshlrev_b32_e32 v58, 16, v60
	v_and_b32_e32 v59, 0xffff0000, v60
	v_lshlrev_b32_e32 v60, 16, v61
	v_and_b32_e32 v61, 0xffff0000, v61
	s_waitcnt vmcnt(0)
	v_lshlrev_b32_e32 v64, 16, v74
	v_and_b32_e32 v65, 0xffff0000, v74
	v_lshlrev_b32_e32 v74, 16, v75
	v_and_b32_e32 v75, 0xffff0000, v75
	v_pk_add_f32 v[60:61], v[60:61], v[74:75]
	v_pk_add_f32 v[58:59], v[58:59], v[64:65]
	v_lshlrev_b32_e32 v74, 16, v62
	v_and_b32_e32 v75, 0xffff0000, v62
	v_lshlrev_b32_e32 v62, 16, v63
	v_and_b32_e32 v63, 0xffff0000, v63
	v_lshlrev_b32_e32 v78, 16, v76
	v_and_b32_e32 v79, 0xffff0000, v76
	v_lshlrev_b32_e32 v64, 16, v77
	v_and_b32_e32 v65, 0xffff0000, v77
	v_pk_add_f32 v[64:65], v[62:63], v[64:65]
	v_pk_add_f32 v[62:63], v[74:75], v[78:79]

.LBB0_1113:
	v_lshlrev_b64 v[50:51], 1, v[58:59]
	v_lshl_add_u64 v[52:53], s[92:93], 0, v[50:51]
	v_lshl_add_u64 v[50:51], s[4:5], 0, v[50:51]
	global_load_dwordx4 v[52:55], v[52:53], off
	s_nop 0
	global_load_dwordx4 v[60:63], v[50:51], off
	s_waitcnt vmcnt(1)
	v_lshlrev_b32_e32 v50, 16, v52
	v_and_b32_e32 v51, 0xffff0000, v52
	v_lshlrev_b32_e32 v52, 16, v53
	v_and_b32_e32 v53, 0xffff0000, v53
	s_waitcnt vmcnt(0)
	v_lshlrev_b32_e32 v56, 16, v60
	v_and_b32_e32 v57, 0xffff0000, v60
	v_lshlrev_b32_e32 v60, 16, v61
	v_and_b32_e32 v61, 0xffff0000, v61
	v_pk_add_f32 v[52:53], v[52:53], v[60:61]
	v_pk_add_f32 v[50:51], v[50:51], v[56:57]
	v_lshlrev_b32_e32 v60, 16, v54
	v_and_b32_e32 v61, 0xffff0000, v54
	v_lshlrev_b32_e32 v54, 16, v55
	v_and_b32_e32 v55, 0xffff0000, v55
	v_lshlrev_b32_e32 v64, 16, v62
	v_and_b32_e32 v65, 0xffff0000, v62
	v_lshlrev_b32_e32 v56, 16, v63
	v_and_b32_e32 v57, 0xffff0000, v63
	v_pk_add_f32 v[56:57], v[54:55], v[56:57]
	v_pk_add_f32 v[54:55], v[60:61], v[64:65]

.LBB0_1116:
	v_lshlrev_b64 v[42:43], 1, v[56:57]
	v_lshl_add_u64 v[44:45], s[92:93], 0, v[42:43]
	v_lshl_add_u64 v[42:43], s[4:5], 0, v[42:43]
	global_load_dwordx4 v[44:47], v[44:45], off
	s_nop 0
	global_load_dwordx4 v[58:61], v[42:43], off
	s_waitcnt vmcnt(1)
	v_lshlrev_b32_e32 v42, 16, v44
	v_and_b32_e32 v43, 0xffff0000, v44
	v_lshlrev_b32_e32 v44, 16, v45
	v_and_b32_e32 v45, 0xffff0000, v45
	s_waitcnt vmcnt(0)
	v_lshlrev_b32_e32 v48, 16, v58
	v_and_b32_e32 v49, 0xffff0000, v58
	v_lshlrev_b32_e32 v58, 16, v59
	v_and_b32_e32 v59, 0xffff0000, v59
	v_pk_add_f32 v[44:45], v[44:45], v[58:59]
	v_pk_add_f32 v[42:43], v[42:43], v[48:49]
	v_lshlrev_b32_e32 v58, 16, v46
	v_and_b32_e32 v59, 0xffff0000, v46
	v_lshlrev_b32_e32 v46, 16, v47
	v_and_b32_e32 v47, 0xffff0000, v47
	v_lshlrev_b32_e32 v62, 16, v60
	v_and_b32_e32 v63, 0xffff0000, v60
	v_lshlrev_b32_e32 v48, 16, v61
	v_and_b32_e32 v49, 0xffff0000, v61
	v_pk_add_f32 v[48:49], v[46:47], v[48:49]
	v_pk_add_f32 v[46:47], v[58:59], v[62:63]

.LBB0_1119:
	v_lshlrev_b64 v[34:35], 1, v[42:43]
	v_lshl_add_u64 v[36:37], s[92:93], 0, v[34:35]
	v_lshl_add_u64 v[34:35], s[4:5], 0, v[34:35]
	global_load_dwordx4 v[36:39], v[36:37], off
	s_nop 0
	global_load_dwordx4 v[44:47], v[34:35], off
	s_waitcnt vmcnt(1)
	v_lshlrev_b32_e32 v34, 16, v36
	v_and_b32_e32 v35, 0xffff0000, v36
	v_lshlrev_b32_e32 v36, 16, v37
	v_and_b32_e32 v37, 0xffff0000, v37
	s_waitcnt vmcnt(0)
	v_lshlrev_b32_e32 v40, 16, v44
	v_and_b32_e32 v41, 0xffff0000, v44
	v_lshlrev_b32_e32 v44, 16, v45
	v_and_b32_e32 v45, 0xffff0000, v45
	v_pk_add_f32 v[36:37], v[36:37], v[44:45]
	v_pk_add_f32 v[34:35], v[34:35], v[40:41]
	v_lshlrev_b32_e32 v44, 16, v38
	v_and_b32_e32 v45, 0xffff0000, v38
	v_lshlrev_b32_e32 v38, 16, v39
	v_and_b32_e32 v39, 0xffff0000, v39
	v_lshlrev_b32_e32 v48, 16, v46
	v_and_b32_e32 v49, 0xffff0000, v46
	v_lshlrev_b32_e32 v40, 16, v47
	v_and_b32_e32 v41, 0xffff0000, v47
	v_pk_add_f32 v[40:41], v[38:39], v[40:41]
	v_pk_add_f32 v[38:39], v[44:45], v[48:49]

.LBB0_1122:
	v_lshlrev_b64 v[26:27], 1, v[40:41]
	v_lshl_add_u64 v[28:29], s[92:93], 0, v[26:27]
	v_lshl_add_u64 v[26:27], s[4:5], 0, v[26:27]
	global_load_dwordx4 v[28:31], v[28:29], off
	s_nop 0
	global_load_dwordx4 v[42:45], v[26:27], off
	s_waitcnt vmcnt(1)
	v_lshlrev_b32_e32 v26, 16, v28
	v_and_b32_e32 v27, 0xffff0000, v28
	v_lshlrev_b32_e32 v28, 16, v29
	v_and_b32_e32 v29, 0xffff0000, v29
	s_waitcnt vmcnt(0)
	v_lshlrev_b32_e32 v32, 16, v42
	v_and_b32_e32 v33, 0xffff0000, v42
	v_lshlrev_b32_e32 v42, 16, v43
	v_and_b32_e32 v43, 0xffff0000, v43
	v_pk_add_f32 v[28:29], v[28:29], v[42:43]
	v_pk_add_f32 v[26:27], v[26:27], v[32:33]
	v_lshlrev_b32_e32 v42, 16, v30
	v_and_b32_e32 v43, 0xffff0000, v30
	v_lshlrev_b32_e32 v30, 16, v31
	v_and_b32_e32 v31, 0xffff0000, v31
	v_lshlrev_b32_e32 v46, 16, v44
	v_and_b32_e32 v47, 0xffff0000, v44
	v_lshlrev_b32_e32 v32, 16, v45
	v_and_b32_e32 v33, 0xffff0000, v45
	v_pk_add_f32 v[32:33], v[30:31], v[32:33]
	v_pk_add_f32 v[30:31], v[42:43], v[46:47]

.LBB0_1125:
	v_lshlrev_b64 v[18:19], 1, v[26:27]
	v_lshl_add_u64 v[20:21], s[92:93], 0, v[18:19]
	v_lshl_add_u64 v[18:19], s[4:5], 0, v[18:19]
	global_load_dwordx4 v[20:23], v[20:21], off
	s_nop 0
	global_load_dwordx4 v[28:31], v[18:19], off
	s_waitcnt vmcnt(1)
	v_lshlrev_b32_e32 v18, 16, v20
	v_and_b32_e32 v19, 0xffff0000, v20
	v_lshlrev_b32_e32 v20, 16, v21
	v_and_b32_e32 v21, 0xffff0000, v21
	s_waitcnt vmcnt(0)
	v_lshlrev_b32_e32 v24, 16, v28
	v_and_b32_e32 v25, 0xffff0000, v28
	v_lshlrev_b32_e32 v28, 16, v29
	v_and_b32_e32 v29, 0xffff0000, v29
	v_pk_add_f32 v[20:21], v[20:21], v[28:29]
	v_pk_add_f32 v[18:19], v[18:19], v[24:25]
	v_lshlrev_b32_e32 v28, 16, v22
	v_and_b32_e32 v29, 0xffff0000, v22
	v_lshlrev_b32_e32 v22, 16, v23
	v_and_b32_e32 v23, 0xffff0000, v23
	v_lshlrev_b32_e32 v32, 16, v30
	v_and_b32_e32 v33, 0xffff0000, v30
	v_lshlrev_b32_e32 v24, 16, v31
	v_and_b32_e32 v25, 0xffff0000, v31
	v_pk_add_f32 v[24:25], v[22:23], v[24:25]
	v_pk_add_f32 v[22:23], v[28:29], v[32:33]
